# indexer pass D: the first three key-block fragment loads are issued before the scan's closing lgkmcnt wait and barrier (their latency overlaps the barrier); on top of v104
# speedup vs baseline: 1.0045x; 1.0045x over previous
; __device__ __forceinline__ void idx_unit(Frame& F, const bf16* QI, const bf16* KI, const float* WI, unsigned* MASK, int b, int j) {
;     ...
;         __syncthreads();
;         ts = __uint_as_float(st[64 + r32]); ti = __uint_as_float(st[96 + r32]); mbase = st[128 + r32];
;     }
;     unsigned short* mrow = (unsigned short*)(MASK + (((size_t)b * 256 + j) * 128) * 64);
;     for (int rd_ = 0; rd_ < 1 + ((IX_DUP >> 1) & 1); ++rd_) { if (rd_) { __syncthreads(); if (F.tid < 32) st[160 + F.tid] = 0u; __syncthreads(); }
.LBB0_1059:
	s_cmp_le_i32 s38, s84
	s_cbranch_scc0 .Lpd_noearly
	s_min_i32 s6, s23, s84
	s_min_i32 s4, s21, s84
	s_ashr_i32 s7, s6, 31
	s_ashr_i32 s5, s4, 31
	s_lshl_b64 s[6:7], s[6:7], 12
	s_lshl_b64 s[4:5], s[4:5], 12
	v_lshl_add_u64 v[8:9], v[218:219], 0, s[6:7]
	v_lshl_add_u64 v[4:5], v[218:219], 0, s[90:91]
	v_lshl_add_u64 v[6:7], v[218:219], 0, s[4:5]
	global_load_dwordx4 v[146:149], v[8:9], off offset:3072
	global_load_dwordx4 v[154:157], v[8:9], off offset:2048
	global_load_dwordx4 v[158:161], v[8:9], off offset:1024
	global_load_dwordx4 v[162:165], v[8:9], off
	global_load_dwordx4 v[68:71], v[6:7], off offset:3072
	global_load_dwordx4 v[72:75], v[6:7], off offset:2048
	global_load_dwordx4 v[76:79], v[6:7], off offset:1024
	global_load_dwordx4 v[150:153], v[6:7], off
	global_load_dwordx4 v[52:55], v[4:5], off offset:3072
	global_load_dwordx4 v[56:59], v[4:5], off offset:2048
	global_load_dwordx4 v[60:63], v[4:5], off offset:1024
	global_load_dwordx4 v[64:67], v[4:5], off
.Lpd_noearly:
	s_add_i32 s4, 0, 0x20080
	s_waitcnt lgkmcnt(0)
	v_lshl_add_u32 v1, v231, 2, s4
	s_barrier
	ds_read2_b32 v[80:81], v1 offset0:64 offset1:96
	ds_read_b32 v1, v1 offset:512
	v_mov_b32_e32 v2, v215
	s_lshl_b32 s4, s76, 23
	s_mov_b32 s85, s93
	s_add_u32 s6, s19, s4
	s_addc_u32 s7, s20, 0
	s_lshl_b64 s[4:5], s[84:85], 15
	s_add_u32 s72, s6, s4
	s_addc_u32 s73, s7, s5
	s_cmp_le_i32 s38, s84
	s_cbranch_scc0 .LBB0_1101
	s_min_i32 s6, s23, s84
	s_min_i32 s4, s21, s84
	s_ashr_i32 s7, s6, 31
	s_ashr_i32 s5, s4, 31
	s_lshl_b64 s[6:7], s[6:7], 12
	s_lshl_b64 s[4:5], s[4:5], 12
	s_branch .Lpd_join

; #define IX_MF(ACC, H, KK) ACC = __builtin_amdgcn_mfma_f32_32x32x16_bf16(a[KK], bq[H][KK], ACC, 0, 0, 0)
; #define IX_RS0(ACC, W, R) do { _Pragma("unroll") for (int r = (R); r < (R) + 4; ++r) { const float x = ACC[r]; sc[r] = __builtin_fmaf(W, IX_RELU(x), 0.0f); } } while (0)
; #define IX_RS(ACC, W, R) do { _Pragma("unroll") for (int r = (R); r < (R) + 4; ++r) { const float x = ACC[r]; sc[r] = __builtin_fmaf(W, IX_RELU(x), sc[r]); } } while (0)
; #define IX_PIN(ACC, VACC, R) asm volatile("" : "+v"(ACC), "+v"(VACC), "+v"(sc[R]), "+v"(sc[(R) + 1]), "+v"(sc[(R) + 2]), "+v"(sc[(R) + 3]))
; template <bool PREV> __device__ __forceinline__ void idx_half1(float (&sc)[16], f32x16& acc0, f32x16& acc1, f32x16& acc2, f32x16& acc3, const bf16x8 (&a)[4], const bf16x8 (&bq)[4][4], const f32x4 wv) {
;     acc0 = (f32x16){};
; #pragma unroll
;     for (int kk = 0; kk < 4; ++kk) { IX_MF(acc0, 0, kk); if constexpr (PREV) { IX_RS(acc2, wv[2], 4 * kk); IX_PIN(acc0, acc2, 4 * kk); } }
;     acc1 = (f32x16){};
; #pragma unroll
;     for (int kk = 0; kk < 4; ++kk) { IX_MF(acc1, 1, kk); if constexpr (PREV) { IX_RS(acc3, wv[3], 4 * kk); IX_PIN(acc1, acc3, 4 * kk); } }
; }
; __device__ __forceinline__ void idx_half2(float (&sc)[16], f32x16& acc0, f32x16& acc1, f32x16& acc2, f32x16& acc3, const bf16x8 (&a)[4], const bf16x8 (&bq)[4][4], const f32x4 wv) {
;     acc2 = (f32x16){};
; #pragma unroll
;     for (int kk = 0; kk < 4; ++kk) { IX_MF(acc2, 2, kk); IX_RS0(acc0, wv[0], 4 * kk); IX_PIN(acc2, acc0, 4 * kk); }
;     acc3 = (f32x16){};
; #pragma unroll
;     for (int kk = 0; kk < 4; ++kk) { IX_MF(acc3, 3, kk); IX_RS(acc1, wv[1], 4 * kk); IX_PIN(acc3, acc1, 4 * kk); }
; }
.Lpd_join:
	s_cmp_gt_i32 s21, s84
	s_waitcnt vmcnt(0)
	v_mfma_f32_32x32x16_bf16 v[20:35], v[64:67], v[82:85], 0
	v_mfma_f32_32x32x16_bf16 v[20:35], v[60:63], v[86:89], v[20:35]
	v_mfma_f32_32x32x16_bf16 v[20:35], v[56:59], v[90:93], v[20:35]
	v_mfma_f32_32x32x16_bf16 v[36:51], v[64:67], v[98:101], 0
	v_mfma_f32_32x32x16_bf16 v[20:35], v[52:55], v[94:97], v[20:35]
	v_mfma_f32_32x32x16_bf16 v[36:51], v[60:63], v[102:105], v[36:51]
	s_nop 10
	v_max_i32_e32 v166, 0, v20
	v_fma_f32 v232, v216, v166, 0
	v_max_i32_e32 v166, 0, v21
	v_fma_f32 v233, v216, v166, 0
	v_max_i32_e32 v166, 0, v22
	v_fma_f32 v234, v216, v166, 0
	v_max_i32_e32 v166, 0, v23
	v_mfma_f32_32x32x16_bf16 v[4:19], v[64:67], v[114:117], 0
	v_fma_f32 v183, v216, v166, 0
	s_nop 0
	v_max_i32_e32 v166, 0, v24
	v_fma_f32 v235, v216, v166, 0
	v_max_i32_e32 v166, 0, v25
	v_fma_f32 v236, v216, v166, 0
	v_mfma_f32_32x32x16_bf16 v[36:51], v[56:59], v[106:109], v[36:51]
	v_max_i32_e32 v166, 0, v26
	v_fma_f32 v237, v216, v166, 0
	v_max_i32_e32 v166, 0, v27
	v_fma_f32 v185, v216, v166, 0
	v_mfma_f32_32x32x16_bf16 v[4:19], v[60:63], v[118:121], v[4:19]
	s_nop 0
	v_max_i32_e32 v166, 0, v28
	v_fma_f32 v238, v216, v166, 0
	v_max_i32_e32 v166, 0, v29
	v_fma_f32 v239, v216, v166, 0
	v_max_i32_e32 v166, 0, v30
	v_mfma_f32_32x32x16_bf16 v[36:51], v[52:55], v[110:113], v[36:51]
	v_fma_f32 v240, v216, v166, 0
	v_max_i32_e32 v166, 0, v31
	v_fma_f32 v187, v216, v166, 0
	v_mfma_f32_32x32x16_bf16 v[4:19], v[56:59], v[122:125], v[4:19]
	s_nop 0
	v_max_i32_e32 v166, 0, v32
	v_fma_f32 v241, v216, v166, 0
	v_max_i32_e32 v166, 0, v33
	v_fma_f32 v242, v216, v166, 0
	v_max_i32_e32 v166, 0, v34
	v_fma_f32 v243, v216, v166, 0
	v_max_i32_e32 v166, 0, v35
	v_mfma_f32_32x32x16_bf16 v[4:19], v[52:55], v[126:129], v[4:19]
	v_fma_f32 v189, v216, v166, 0
	s_nop 0
	v_mfma_f32_32x32x16_bf16 v[20:35], v[64:67], v[130:133], 0
	v_max_i32_e32 v64, 0, v36
	v_fmac_f32_e32 v232, v217, v64
	v_max_i32_e32 v64, 0, v37
	v_fmac_f32_e32 v233, v217, v64
	v_max_i32_e32 v64, 0, v38
	v_fmac_f32_e32 v234, v217, v64
	v_max_i32_e32 v64, 0, v39
	v_fmac_f32_e32 v183, v217, v64
	s_nop 0
	v_mfma_f32_32x32x16_bf16 v[20:35], v[60:63], v[134:137], v[20:35]
	v_max_i32_e32 v60, 0, v40
	v_fmac_f32_e32 v235, v217, v60
	v_max_i32_e32 v60, 0, v41
	v_fmac_f32_e32 v236, v217, v60
	v_max_i32_e32 v60, 0, v42
	v_fmac_f32_e32 v237, v217, v60
	v_max_i32_e32 v60, 0, v43
	v_fmac_f32_e32 v185, v217, v60
	s_nop 0
	v_mfma_f32_32x32x16_bf16 v[20:35], v[56:59], v[138:141], v[20:35]
	v_max_i32_e32 v56, 0, v44
	v_fmac_f32_e32 v238, v217, v56
	v_max_i32_e32 v56, 0, v45
	v_fmac_f32_e32 v239, v217, v56
	v_max_i32_e32 v56, 0, v46
	v_fmac_f32_e32 v240, v217, v56
	v_max_i32_e32 v56, 0, v47
	v_fmac_f32_e32 v187, v217, v56
	s_nop 0
	v_mfma_f32_32x32x16_bf16 v[20:35], v[52:55], v[142:145], v[20:35]
	v_max_i32_e32 v52, 0, v48
	v_fmac_f32_e32 v241, v217, v52
	v_max_i32_e32 v52, 0, v49
	v_fmac_f32_e32 v242, v217, v52
	v_max_i32_e32 v52, 0, v50
	v_fmac_f32_e32 v243, v217, v52
	v_max_i32_e32 v52, 0, v51
	v_fmac_f32_e32 v189, v217, v52
	s_cbranch_scc1 .LBB0_1090
	v_lshlrev_b32_e32 v215, 2, v230
	v_or_b32_e32 v38, 2, v215
	v_cmp_gt_i32_e64 s[44:45], v38, v231
	v_or_b32_e32 v38, 3, v215
	v_cmp_gt_i32_e64 s[46:47], v38, v231
	v_add_u32_e32 v38, 8, v215
	v_cmp_gt_i32_e64 s[48:49], v38, v231
	v_add_u32_e32 v38, 9, v215
	v_cmp_gt_i32_e64 s[50:51], v38, v231
	v_add_u32_e32 v38, 10, v215
	v_cmp_gt_i32_e64 s[52:53], v38, v231
	v_add_u32_e32 v38, 11, v215
	v_cmp_gt_i32_e64 s[54:55], v38, v231
	v_add_u32_e32 v38, 16, v215
	v_cmp_gt_i32_e64 s[56:57], v38, v231
	v_add_u32_e32 v38, 17, v215
	v_cmp_gt_i32_e64 s[58:59], v38, v231
	v_add_u32_e32 v38, 18, v215
	v_cmp_gt_i32_e64 s[60:61], v38, v231
	v_add_u32_e32 v38, 19, v215
	v_cmp_gt_i32_e64 s[62:63], v38, v231
	v_add_u32_e32 v38, 24, v215
	v_cmp_gt_i32_e64 s[64:65], v38, v231
	v_add_u32_e32 v38, 25, v215
	v_readlane_b32 s4, v252, 35
	v_ashrrev_i32_e32 v213, 31, v212
	v_cmp_gt_i32_e64 s[66:67], v38, v231
	v_add_u32_e32 v38, 26, v215
	s_min_i32 s74, s4, s84
	v_lshl_add_u64 v[36:37], v[212:213], 2, s[72:73]
	s_add_i32 s4, 0, 0x20300
	v_cmp_gt_i32_e64 s[68:69], v38, v231
	v_add_u32_e32 v38, 27, v215
	s_mov_b32 s97, s93
	v_lshl_add_u32 v213, v231, 2, s4
	v_cmp_gt_i32_e64 s[40:41], v215, v231
	v_cmp_lt_i32_e64 s[42:43], v215, v231
	v_cmp_gt_i32_e64 s[70:71], v38, v231
	v_lshl_add_u64 v[190:191], v[36:37], 0, s[96:97]
	s_mov_b32 s97, s38
	s_mov_b32 s85, s21
	s_branch .LBB0_1064
